# L0 prologue: Whh0 loads issued before the drain (counted vmcnt(16)), Wih0/bias loads exec-masked sharing VGPRs, alloc 128
# speedup vs baseline: 1.0154x; 1.0009x over previous
.LBB1_400:
	s_andn2_b64 vcc, exec, s[6:7]
	s_cbranch_vccnz .LBB1_434
	v_lshlrev_b32_e32 v34, 4, v0
	v_mov_b32_e32 v35, 0
	v_lshl_add_u64 v[2:3], s[28:29], 0, v[34:35]
	v_add_co_u32_e32 v4, vcc, 0x3000, v2
	s_load_dwordx8 s[4:11], s[0:1], 0x8
	s_nop 0
	v_addc_co_u32_e32 v5, vcc, 0, v3, vcc
	v_add_co_u32_e32 v6, vcc, 0x6000, v2
	v_or_b32_e32 v107, 0xc00, v0
	s_nop 0
	v_addc_co_u32_e32 v7, vcc, 0, v3, vcc
	v_add_co_u32_e32 v2, vcc, 0x9000, v2
	global_load_dwordx4 v[68:71], v34, s[28:29]
	s_nop 0
	v_addc_co_u32_e32 v3, vcc, 0, v3, vcc
	global_load_dwordx4 v[30:33], v[4:5], off
	global_load_dwordx4 v[26:29], v[6:7], off
	v_lshlrev_b32_e32 v4, 4, v107
	global_load_dwordx4 v[22:25], v[2:3], off
	global_load_dwordx4 v[18:21], v4, s[28:29]
	v_and_b32_e32 v6, 3, v0
	v_bfe_u32 v2, v0, 2, 2
	v_lshl_or_b32 v2, v6, 6, v2
	v_lshl_or_b32 v14, s68, 4, v2
	v_lshrrev_b32_e32 v1, 4, v106
	v_mov_b32_e32 v2, 0xbfb8aa3b
	v_mov_b32_e32 v3, 0xc038aa3b
	v_cmp_eq_u32_e32 vcc, 2, v6
	v_cmp_gt_u32_e64 s[2:3], 16, v106
	v_lshlrev_b32_e32 v34, 5, v14
	v_cndmask_b32_e32 v104, v2, v3, vcc
	v_lshlrev_b32_e32 v35, 2, v14
	v_lshlrev_b32_e32 v107, 8, v14
	v_mov_b32_e32 v105, v104
	v_lshl_add_u32 v107, v1, 5, v107
	v_cmp_eq_u32_e64 s[12:13], 1, v1
	v_mov_b32_e32 v2, 0
	v_mov_b32_e32 v3, 0
	v_mov_b32_e32 v4, 0
	v_mov_b32_e32 v5, 0
	v_mov_b32_e32 v6, 0
	v_mov_b32_e32 v7, 0
	v_mov_b32_e32 v8, 0
	v_mov_b32_e32 v9, 0
	v_mov_b32_e32 v10, 0
	v_mov_b32_e32 v11, 0
	v_mov_b32_e32 v12, 0
	v_mov_b32_e32 v13, 0
	v_mov_b32_e32 v14, 0
	v_mov_b32_e32 v15, 0
	v_mov_b32_e32 v16, 0
	v_mov_b32_e32 v17, 0
	s_waitcnt lgkmcnt(0)
	s_mov_b64 exec, s[2:3]
	global_load_dwordx4 v[2:5], v34, s[4:5]
	global_load_dwordx4 v[112:115], v34, s[4:5] offset:16
	global_load_dwordx4 v[6:9], v34, s[4:5] offset:128
	global_load_dwordx4 v[116:119], v34, s[4:5] offset:144
	global_load_dwordx4 v[10:13], v34, s[4:5] offset:256
	global_load_dwordx4 v[120:123], v34, s[4:5] offset:272
	global_load_dwordx4 v[14:17], v34, s[4:5] offset:384
	global_load_dwordx4 v[124:127], v34, s[4:5] offset:400
	s_mov_b64 exec, s[12:13]
	global_load_dword v112, v35, s[8:9]
	global_load_dword v113, v35, s[10:11]
	global_load_dword v116, v35, s[8:9] offset:16
	global_load_dword v117, v35, s[10:11] offset:16
	global_load_dword v120, v35, s[8:9] offset:32
	global_load_dword v121, v35, s[10:11] offset:32
	global_load_dword v124, v35, s[8:9] offset:48
	global_load_dword v125, v35, s[10:11] offset:48
	s_mov_b64 exec, -1
	global_load_dwordx4 v[44:47], v107, s[6:7] offset:16
	global_load_dwordx4 v[56:59], v107, s[6:7]
	global_load_dwordx4 v[48:51], v107, s[6:7] offset:144
	global_load_dwordx4 v[52:55], v107, s[6:7] offset:128
	global_load_dwordx4 v[36:39], v107, s[6:7] offset:1040
	global_load_dwordx4 v[64:67], v107, s[6:7] offset:1024
	global_load_dwordx4 v[40:43], v107, s[6:7] offset:1168
	global_load_dwordx4 v[60:63], v107, s[6:7] offset:1152
	global_load_dwordx4 v[80:83], v107, s[6:7] offset:2064
	global_load_dwordx4 v[84:87], v107, s[6:7] offset:2048
	global_load_dwordx4 v[72:75], v107, s[6:7] offset:2192
	global_load_dwordx4 v[76:79], v107, s[6:7] offset:2176
	global_load_dwordx4 v[96:99], v107, s[6:7] offset:3088
	global_load_dwordx4 v[100:103], v107, s[6:7] offset:3072
	global_load_dwordx4 v[88:91], v107, s[6:7] offset:3216
	global_load_dwordx4 v[92:95], v107, s[6:7] offset:3200
	v_or_b32_e32 v107, 0xc00, v0
	s_waitcnt vmcnt(16)
	s_mov_b64 exec, s[2:3]
	v_fma_mixlo_f16 v111, v104, v2, 0
	v_mul_f32_e32 v3, v104, v3
	v_mul_f32_e32 v4, v104, v4
	v_mul_f32_e32 v5, v104, v5
	v_mul_f32_e32 v112, v104, v112
	v_mul_f32_e32 v113, v104, v113
	v_mul_f32_e32 v114, v104, v114
	v_cvt_pk_f16_f32 v3, v3, v4
	v_cvt_pk_f16_f32 v112, v5, v112
	v_cvt_pk_f16_f32 v113, v113, v114
	v_pack_b32_f16 v2, v111, v3
	v_alignbit_b32 v3, v112, v3, 16
	v_alignbit_b32 v4, v113, v112, 16
	v_lshrrev_b32_e32 v5, 16, v113
	v_fma_mixhi_f16 v5, v104, v115, 0
	v_fma_mixlo_f16 v111, v104, v6, 0
	v_mul_f32_e32 v7, v104, v7
	v_mul_f32_e32 v8, v104, v8
	v_mul_f32_e32 v9, v104, v9
	v_mul_f32_e32 v116, v104, v116
	v_mul_f32_e32 v117, v104, v117
	v_mul_f32_e32 v118, v104, v118
	v_cvt_pk_f16_f32 v7, v7, v8
	v_cvt_pk_f16_f32 v116, v9, v116
	v_cvt_pk_f16_f32 v117, v117, v118
	v_pack_b32_f16 v6, v111, v7
	v_alignbit_b32 v7, v116, v7, 16
	v_alignbit_b32 v8, v117, v116, 16
	v_lshrrev_b32_e32 v9, 16, v117
	v_fma_mixhi_f16 v9, v104, v119, 0
	v_fma_mixlo_f16 v111, v104, v10, 0
	v_mul_f32_e32 v11, v104, v11
	v_mul_f32_e32 v12, v104, v12
	v_mul_f32_e32 v13, v104, v13
	v_mul_f32_e32 v120, v104, v120
	v_mul_f32_e32 v121, v104, v121
	v_mul_f32_e32 v122, v104, v122
	v_cvt_pk_f16_f32 v11, v11, v12
	v_cvt_pk_f16_f32 v120, v13, v120
	v_cvt_pk_f16_f32 v121, v121, v122
	v_pack_b32_f16 v10, v111, v11
	v_alignbit_b32 v11, v120, v11, 16
	v_alignbit_b32 v12, v121, v120, 16
	v_lshrrev_b32_e32 v13, 16, v121
	v_fma_mixhi_f16 v13, v104, v123, 0
	v_fma_mixlo_f16 v111, v104, v14, 0
	v_mul_f32_e32 v15, v104, v15
	v_mul_f32_e32 v16, v104, v16
	v_mul_f32_e32 v17, v104, v17
	v_mul_f32_e32 v124, v104, v124
	v_mul_f32_e32 v125, v104, v125
	v_mul_f32_e32 v126, v104, v126
	v_cvt_pk_f16_f32 v15, v15, v16
	v_cvt_pk_f16_f32 v124, v17, v124
	v_cvt_pk_f16_f32 v125, v125, v126
	v_pack_b32_f16 v14, v111, v15
	v_alignbit_b32 v15, v124, v15, 16
	v_alignbit_b32 v16, v125, v124, 16
	v_lshrrev_b32_e32 v17, 16, v125
	v_fma_mixhi_f16 v17, v104, v127, 0
	s_mov_b64 exec, s[12:13]
	s_mov_b32 s14, 0xffff
	v_add_f32_e32 v111, v112, v113
	v_fma_mixlo_f16 v111, v104, v111, 0
	v_bfi_b32 v2, s14, v111, v2
	v_add_f32_e32 v111, v116, v117
	v_fma_mixlo_f16 v111, v104, v111, 0
	v_bfi_b32 v6, s14, v111, v6
	v_add_f32_e32 v111, v120, v121
	v_fma_mixlo_f16 v111, v104, v111, 0
	v_bfi_b32 v10, s14, v111, v10
	v_add_f32_e32 v111, v124, v125
	v_fma_mixlo_f16 v111, v104, v111, 0
	v_bfi_b32 v14, s14, v111, v14
	s_mov_b64 exec, -1
	v_cmp_eq_u32_e32 vcc, 1, v1
	v_mul_u32_u24_e32 v110, 0x556, v0
	v_lshrrev_b32_e32 v110, 16, v110
	v_mul_lo_u16_e32 v111, 48, v110
	v_sub_u16_e32 v111, v0, v111
	v_lshrrev_b32_e32 v112, 1, v111
	s_waitcnt vmcnt(20)
	v_cvt_pk_f16_f32 v71, v70, v71
	v_cvt_pk_f16_f32 v70, v68, v69
	s_movk_i32 s4, 0x50
	v_lshlrev_b32_e32 v69, 3, v111
	v_mad_u32_u24 v68, v112, s4, v110
	v_and_b32_e32 v69, 8, v69
	v_lshl_or_b32 v68, v68, 4, v69
	v_add_u32_e32 v35, 0x300, v0
	v_add_u32_e32 v68, 0x14000, v68
	ds_write_b64 v68, v[70:71]
	v_mul_u32_u24_e32 v68, 0x556, v35
	v_lshrrev_b32_e32 v68, 16, v68
	v_mul_lo_u16_e32 v69, 48, v68
	v_sub_u16_e32 v35, v35, v69
	v_lshrrev_b32_e32 v69, 1, v35
	s_waitcnt vmcnt(19)
	v_cvt_pk_f16_f32 v33, v32, v33
	v_cvt_pk_f16_f32 v32, v30, v31
	v_lshlrev_b32_e32 v31, 3, v35
	v_mad_u32_u24 v30, v69, s4, v68
	v_and_b32_e32 v31, 8, v31
	v_lshl_or_b32 v30, v30, 4, v31
	v_add_u32_e32 v108, 0x600, v0
	v_add_u32_e32 v30, 0x14000, v30
	ds_write_b64 v30, v[32:33]
	v_mul_u32_u24_e32 v30, 0xaab, v108
	v_lshrrev_b32_e32 v30, 17, v30
	v_mul_lo_u16_e32 v31, 48, v30
	v_sub_u16_e32 v31, v108, v31
	v_lshrrev_b32_e32 v32, 1, v31
	s_waitcnt vmcnt(18)
	v_cvt_pk_f16_f32 v29, v28, v29
	v_cvt_pk_f16_f32 v28, v26, v27
	v_lshlrev_b32_e32 v27, 3, v31
	v_mad_u32_u24 v26, v32, s4, v30
	v_and_b32_e32 v27, 8, v27
	v_lshl_or_b32 v26, v26, 4, v27
	v_add_u32_e32 v109, 0x900, v0
	v_add_u32_e32 v26, 0x14000, v26
	ds_write_b64 v26, v[28:29]
	v_mul_u32_u24_e32 v26, 0xaab, v109
	v_lshrrev_b32_e32 v26, 17, v26
	v_mul_lo_u16_e32 v27, 48, v26
	v_sub_u16_e32 v27, v109, v27
	v_lshrrev_b32_e32 v28, 1, v27
	s_waitcnt vmcnt(17)
	v_cvt_pk_f16_f32 v25, v24, v25
	v_cvt_pk_f16_f32 v24, v22, v23
	v_lshlrev_b32_e32 v23, 3, v27
	v_mad_u32_u24 v22, v28, s4, v26
	v_and_b32_e32 v23, 8, v23
	v_lshl_or_b32 v22, v22, 4, v23
	v_add_u32_e32 v22, 0x14000, v22
	ds_write_b64 v22, v[24:25]
	v_mul_u32_u24_e32 v22, 0xaab, v107
	v_lshrrev_b32_e32 v22, 17, v22
	v_mul_lo_u16_e32 v23, 48, v22
	v_sub_u16_e32 v23, v107, v23
	v_lshrrev_b32_e32 v24, 1, v23
	s_waitcnt vmcnt(16)
	v_cvt_pk_f16_f32 v21, v20, v21
	v_cvt_pk_f16_f32 v20, v18, v19
	v_lshlrev_b32_e32 v19, 3, v23
	v_mad_u32_u24 v18, v24, s4, v22
	v_and_b32_e32 v19, 8, v19
	v_lshl_or_b32 v18, v18, 4, v19
	s_movk_i32 s4, 0x9f
	v_add_u32_e32 v18, 0x14000, v18
	v_cmp_lt_u32_e64 s[4:5], s4, v0
	ds_write_b64 v18, v[20:21]
	s_and_saveexec_b64 s[6:7], s[4:5]
	s_xor_b64 s[4:5], exec, s[6:7]
	v_lshlrev_b32_e32 v34, 4, v0
	s_andn2_saveexec_b64 s[6:7], s[4:5]
	s_cbranch_execz .LBB1_421
	s_movk_i32 s4, 0x50
	v_mov_b32_e32 v18, 0x3c00
	v_cmp_gt_u32_e64 s[4:5], s4, v0
	v_mov_b32_e32 v19, 0
	v_add_u32_e32 v22, 0x1b800, v34
	v_cndmask_b32_e64 v18, 0, v18, s[4:5]
	v_mov_b32_e32 v20, v19
	v_mov_b32_e32 v21, v19
	ds_write_b128 v22, v[18:21]

	.amdhsa_kernel _Z11k_lstm_mfmaPKfS0_S0_S0_S0_S0_S0_S0_S0_Pf6WkArgs
		.amdhsa_group_segment_fixed_size 134696
		.amdhsa_private_segment_fixed_size 0
		.amdhsa_kernarg_size 488
		.amdhsa_user_sgpr_count 2
		.amdhsa_user_sgpr_dispatch_ptr 0
		.amdhsa_user_sgpr_queue_ptr 0
		.amdhsa_user_sgpr_kernarg_segment_ptr 1
		.amdhsa_user_sgpr_dispatch_id 0
		.amdhsa_user_sgpr_kernarg_preload_length 0
		.amdhsa_user_sgpr_kernarg_preload_offset 0
		.amdhsa_user_sgpr_private_segment_size 0
		.amdhsa_uses_dynamic_stack 0
		.amdhsa_enable_private_segment 0
		.amdhsa_system_sgpr_workgroup_id_x 1
		.amdhsa_system_sgpr_workgroup_id_y 0
		.amdhsa_system_sgpr_workgroup_id_z 0
		.amdhsa_system_sgpr_workgroup_info 0
		.amdhsa_system_vgpr_workitem_id 0
		.amdhsa_next_free_vgpr 128
		.amdhsa_next_free_sgpr 96
		.amdhsa_accum_offset 128
		.amdhsa_reserve_vcc 1
		.amdhsa_float_round_mode_32 0
		.amdhsa_float_round_mode_16_64 0
		.amdhsa_float_denorm_mode_32 3
		.amdhsa_float_denorm_mode_16_64 3
		.amdhsa_dx10_clamp 1
		.amdhsa_ieee_mode 1
		.amdhsa_fp16_overflow 0
		.amdhsa_tg_split 0
		.amdhsa_exception_fp_ieee_invalid_op 0
		.amdhsa_exception_fp_denorm_src 0
		.amdhsa_exception_fp_ieee_div_zero 0
		.amdhsa_exception_fp_ieee_overflow 0
		.amdhsa_exception_fp_ieee_underflow 0
		.amdhsa_exception_fp_ieee_inexact 0
		.amdhsa_exception_int_div_zero 0
	.end_amdhsa_kernel

amdhsa.kernels:
  - .agpr_count:     0
    .args:
      - .actual_access:  read_only
        .address_space:  global
        .offset:         0
        .size:           8
        .value_kind:     global_buffer
      - .actual_access:  read_only
        .address_space:  global
        .offset:         8
        .size:           8
        .value_kind:     global_buffer
      - .actual_access:  read_only
        .address_space:  global
        .offset:         16
        .size:           8
        .value_kind:     global_buffer
      - .actual_access:  read_only
        .address_space:  global
        .offset:         24
        .size:           8
        .value_kind:     global_buffer
      - .actual_access:  read_only
        .address_space:  global
        .offset:         32
        .size:           8
        .value_kind:     global_buffer
      - .actual_access:  read_only
        .address_space:  global
        .offset:         40
        .size:           8
        .value_kind:     global_buffer
      - .actual_access:  read_only
        .address_space:  global
        .offset:         48
        .size:           8
        .value_kind:     global_buffer
      - .actual_access:  read_only
        .address_space:  global
        .offset:         56
        .size:           8
        .value_kind:     global_buffer
      - .actual_access:  write_only
        .address_space:  global
        .offset:         64
        .size:           8
        .value_kind:     global_buffer
      - .actual_access:  write_only
        .address_space:  global
        .offset:         72
        .size:           8
        .value_kind:     global_buffer
      - .actual_access:  write_only
        .address_space:  global
        .offset:         80
        .size:           8
        .value_kind:     global_buffer
      - .actual_access:  write_only
        .address_space:  global
        .offset:         88
        .size:           8
        .value_kind:     global_buffer
      - .address_space:  global
        .offset:         96
        .size:           8
        .value_kind:     global_buffer
      - .address_space:  global
        .offset:         104
        .size:           8
        .value_kind:     global_buffer
      - .address_space:  global
        .offset:         112
        .size:           8
        .value_kind:     global_buffer
      - .address_space:  global
        .offset:         120
        .size:           8
        .value_kind:     global_buffer
      - .actual_access:  read_only
        .address_space:  global
        .offset:         128
        .size:           8
        .value_kind:     global_buffer
      - .actual_access:  write_only
        .address_space:  global
        .offset:         136
        .size:           8
        .value_kind:     global_buffer
    .group_segment_fixed_size: 84096
    .kernarg_segment_align: 8
    .kernarg_segment_size: 144
    .language:       OpenCL C
    .language_version:
      - 2
      - 0
    .max_flat_workgroup_size: 1024
    .name:           _Z14k_csr_fallbackPKiS0_S0_PKfS2_S2_S2_S2_PDv8_DF16_S4_S4_S4_PiS5_PfS4_S2_PDF16_
    .private_segment_fixed_size: 0
    .sgpr_count:     50
    .sgpr_spill_count: 0
    .symbol:         _Z14k_csr_fallbackPKiS0_S0_PKfS2_S2_S2_S2_PDv8_DF16_S4_S4_S4_PiS5_PfS4_S2_PDF16_.kd
    .uniform_work_group_size: 1
    .uses_dynamic_stack: false
    .vgpr_count:     93
    .vgpr_spill_count: 0
    .wavefront_size: 64
  - .agpr_count:     0
    .args:
      - .actual_access:  read_only
        .address_space:  global
        .offset:         0
        .size:           8
        .value_kind:     global_buffer
      - .actual_access:  read_only
        .address_space:  global
        .offset:         8
        .size:           8
        .value_kind:     global_buffer
      - .actual_access:  read_only
        .address_space:  global
        .offset:         16
        .size:           8
        .value_kind:     global_buffer
      - .actual_access:  read_only
        .address_space:  global
        .offset:         24
        .size:           8
        .value_kind:     global_buffer
      - .actual_access:  read_only
        .address_space:  global
        .offset:         32
        .size:           8
        .value_kind:     global_buffer
      - .actual_access:  read_only
        .address_space:  global
        .offset:         40
        .size:           8
        .value_kind:     global_buffer
      - .actual_access:  read_only
        .address_space:  global
        .offset:         48
        .size:           8
        .value_kind:     global_buffer
      - .actual_access:  read_only
        .address_space:  global
        .offset:         56
        .size:           8
        .value_kind:     global_buffer
      - .actual_access:  read_only
        .address_space:  global
        .offset:         64
        .size:           8
        .value_kind:     global_buffer
      - .actual_access:  write_only
        .address_space:  global
        .offset:         72
        .size:           8
        .value_kind:     global_buffer
      - .offset:         80
        .size:           152
        .value_kind:     by_value
      - .offset:         232
        .size:           4
        .value_kind:     hidden_block_count_x
      - .offset:         236
        .size:           4
        .value_kind:     hidden_block_count_y
      - .offset:         240
        .size:           4
        .value_kind:     hidden_block_count_z
      - .offset:         244
        .size:           2
        .value_kind:     hidden_group_size_x
      - .offset:         246
        .size:           2
        .value_kind:     hidden_group_size_y
      - .offset:         248
        .size:           2
        .value_kind:     hidden_group_size_z
      - .offset:         250
        .size:           2
        .value_kind:     hidden_remainder_x
      - .offset:         252
        .size:           2
        .value_kind:     hidden_remainder_y
      - .offset:         254
        .size:           2
        .value_kind:     hidden_remainder_z
      - .offset:         272
        .size:           8
        .value_kind:     hidden_global_offset_x
      - .offset:         280
        .size:           8
        .value_kind:     hidden_global_offset_y
      - .offset:         288
        .size:           8
        .value_kind:     hidden_global_offset_z
      - .offset:         296
        .size:           2
        .value_kind:     hidden_grid_dims
    .group_segment_fixed_size: 134696
    .kernarg_segment_align: 8
    .kernarg_segment_size: 488
    .language:       OpenCL C
    .language_version:
      - 2
      - 0
    .max_flat_workgroup_size: 1024
    .name:           _Z11k_lstm_mfmaPKfS0_S0_S0_S0_S0_S0_S0_S0_Pf6WkArgs
    .private_segment_fixed_size: 0
    .sgpr_count:     76
    .sgpr_spill_count: 0
    .symbol:         _Z11k_lstm_mfmaPKfS0_S0_S0_S0_S0_S0_S0_S0_Pf6WkArgs.kd
    .uniform_work_group_size: 1
    .uses_dynamic_stack: false
    .vgpr_count:     128
    .vgpr_spill_count: 0
    .wavefront_size: 64
  - .agpr_count:     0
    .args:
      - .actual_access:  read_only
        .address_space:  global
        .offset:         0
        .size:           8
        .value_kind:     global_buffer
      - .actual_access:  read_only
        .address_space:  global
        .offset:         8
        .size:           8
        .value_kind:     global_buffer
      - .actual_access:  read_only
        .address_space:  global
        .offset:         16
        .size:           8
        .value_kind:     global_buffer
      - .actual_access:  read_only
        .address_space:  global
        .offset:         24
        .size:           8
        .value_kind:     global_buffer
      - .actual_access:  read_only
        .address_space:  global
        .offset:         32
        .size:           8
        .value_kind:     global_buffer
      - .actual_access:  read_only
        .address_space:  global
        .offset:         40
        .size:           8
        .value_kind:     global_buffer
      - .actual_access:  read_only
        .address_space:  global
        .offset:         48
        .size:           8
        .value_kind:     global_buffer
      - .actual_access:  read_only
        .address_space:  global
        .offset:         56
        .size:           8
        .value_kind:     global_buffer
      - .actual_access:  read_only
        .address_space:  global
        .offset:         64
        .size:           8
        .value_kind:     global_buffer
      - .actual_access:  read_only
        .address_space:  global
        .offset:         72
        .size:           8
        .value_kind:     global_buffer
      - .actual_access:  read_only
        .address_space:  global
        .offset:         80
        .size:           8
        .value_kind:     global_buffer
      - .actual_access:  read_only
        .address_space:  global
        .offset:         88
        .size:           8
        .value_kind:     global_buffer
      - .actual_access:  read_only
        .address_space:  global
        .offset:         96
        .size:           8
        .value_kind:     global_buffer
      - .actual_access:  read_only
        .address_space:  global
        .offset:         104
        .size:           8
        .value_kind:     global_buffer
      - .actual_access:  read_only
        .address_space:  global
        .offset:         112
        .size:           8
        .value_kind:     global_buffer
      - .actual_access:  write_only
        .address_space:  global
        .offset:         120
        .size:           8
        .value_kind:     global_buffer
      - .actual_access:  read_only
        .address_space:  global
        .offset:         128
        .size:           8
        .value_kind:     global_buffer
    .group_segment_fixed_size: 12288
    .kernarg_segment_align: 8
    .kernarg_segment_size: 136
    .language:       OpenCL C
    .language_version:
      - 2
      - 0
    .max_flat_workgroup_size: 256
    .name:           _Z5k_gcnILi128ELb1ELi16EEvPKDv8_DF16_PKiS4_PKfS2_S6_PDF16_S6_S6_S2_S6_S2_S6_S6_S6_PfS4_
    .private_segment_fixed_size: 0
    .sgpr_count:     48
    .sgpr_spill_count: 0
    .symbol:         _Z5k_gcnILi128ELb1ELi16EEvPKDv8_DF16_PKiS4_PKfS2_S6_PDF16_S6_S6_S2_S6_S2_S6_S6_S6_PfS4_.kd
    .uniform_work_group_size: 1
    .uses_dynamic_stack: false
    .vgpr_count:     96
    .vgpr_spill_count: 0
    .wavefront_size: 64
